# grid barrier: one signalling stage (XCD-last workgroup adds to a monotonic top counter without a return value, every workgroup polls it) instead of top + per-XCD generation words
# baseline (speedup 1.0000x reference)
; #define CAS __attribute__((address_space(4)))
;     template <class T> __device__ __forceinline__ T* w(size_t off) const { return (T*)(p->ws + off); }
; __global__ void __launch_bounds__(NTHR, 2) mk_fwd(Params prm) {
;     __shared__ __attribute__((aligned(16))) unsigned char smem_raw[S3_LDS_END];
;     float* smem = (float*)(smem_raw + GEMM_LDS);
;     Ctx c; c.p = (const CAS Params*)__builtin_amdgcn_kernarg_segment_ptr(); c.smf = smem; c.tid = threadIdx.x;
;     const int G = gridDim.x, bid = blockIdx.x;
;     const int gthreads = G * NTHR, nwaves = gthreads >> 6;
;     ...
;     int* smi = (int*)(smem + 16);
;     ...
;     volatile unsigned* bst = (volatile unsigned*)(smem + 120);
;     if (c.tid == 0) { bst[0] = 0u; bst[1] = 0u; }
;     __syncthreads();
;     XcdBarrier bar = xcd_barrier_post(c.w<unsigned>(WS_CTL) + CW_BAR, bst);
_ZN12_GLOBAL__N_16mk_fwdENS_6ParamsE:
	v_mov_b32_e32 v255, 0
	s_load_dword s3, s[0:1], 0x140
	s_add_u32 s4, s0, 0x140
	v_writelane_b32 v253, s2, 0
	s_addc_u32 s5, s1, 0
	v_writelane_b32 v253, s4, 1
	v_cmp_eq_u32_e64 s[6:7], 0, v0
	s_nop 0
	v_writelane_b32 v253, s5, 2
	s_mov_b64 s[4:5], exec
	v_writelane_b32 v253, s6, 3
	s_nop 1
	v_writelane_b32 v253, s7, 4
	s_and_b64 s[6:7], s[4:5], s[6:7]
	s_mov_b64 exec, s[6:7]
	s_cbranch_execz .LBB0_2
	s_mov_b64 s[6:7], src_shared_base
	v_mov_b32_e32 v2, 0x8de0
	v_mov_b32_e32 v3, s7
	v_mov_b32_e32 v1, 0
	flat_store_dword v[2:3], v1 sc0 sc1
	s_waitcnt vmcnt(0)
	v_mov_b32_e32 v2, 0x8de4
	flat_store_dword v[2:3], v1 sc0 sc1
	s_waitcnt vmcnt(0)

; __device__ __forceinline__ unsigned xb_ld(unsigned* p)              { return __hip_atomic_load(p, __ATOMIC_RELAXED, __HIP_MEMORY_SCOPE_AGENT); }
; __device__ __forceinline__ unsigned xb_add(unsigned* p, unsigned v) { return __hip_atomic_fetch_add(p, v, __ATOMIC_RELAXED, __HIP_MEMORY_SCOPE_AGENT); }
; #define XB_SPIN(cond, bar) do { unsigned _sp = 0; while (cond) { __builtin_amdgcn_s_sleep(1); \
;     if ((++_sp & 255u) == 0u) { if (xb_ld(&(bar)[XB_TMO])) break; if (_sp > XB_SPIN_CAP) { atomicAdd(&(bar)[XB_TMO], 1u); break; } } } } while (0)
; __device__ __forceinline__ void xcd_barrier(const XcdBarrier& b) {
;     asm volatile("s_waitcnt vmcnt(0)" ::: "memory");
;     __syncthreads();
;     if (threadIdx.x == 0) {
;         unsigned* bar = b.bar;
;         __builtin_amdgcn_s_waitcnt(0);
;         unsigned nloc = b.st[0], nx = b.st[1];
;         if (nloc == 0u) { xcd_barrier_complete(bar, b.x, nloc, nx); b.st[0] = nloc; b.st[1] = nx; }
;         const unsigned old = xb_add(&bar[XB_XSUB(b.x)], 1u);
;         const unsigned gen = old / nloc;
;         if (old + 1u == (gen + 1u) * nloc) {
;             __builtin_amdgcn_fence(__ATOMIC_RELEASE, "agent");
;             asm volatile("s_waitcnt vmcnt(0)" ::: "memory");
;             const unsigned og = xb_add(&bar[XB_TOP], 1u);
;             const unsigned tg = og / nx;
;             if (og + 1u == (tg + 1u) * nx) xb_add(&bar[XB_TOPGEN], 1u);
;             else XB_SPIN(xb_ld(&bar[XB_TOPGEN]) == tg, bar);
;             __builtin_amdgcn_fence(__ATOMIC_ACQUIRE, "agent");
;             xb_add(&bar[XB_XGEN(b.x)], 1u);
;             asm volatile("s_waitcnt vmcnt(0)" ::: "memory");
;         } else {
;             XB_SPIN(xb_ld(&bar[XB_XGEN(b.x)]) == gen, bar);
;             __builtin_amdgcn_fence(__ATOMIC_ACQUIRE, "agent");
;             asm volatile("s_waitcnt vmcnt(0)" ::: "memory");
;         }
;     }
;     __syncthreads();
; }
.LBB0_726:
	s_or_b64 exec, exec, s[28:29]
	v_readlane_b32 s16, v252, 40
	v_readlane_b32 s17, v252, 41
	v_readlane_b32 s6, v252, 44
	v_readlane_b32 s7, v252, 45
	v_mov_b32_e32 v6, 1
	v_add_u32_e32 v255, 1, v255
	s_nop 2
	global_atomic_add v6, v3, v6, s[16:17] sc0
	v_mul_lo_u32 v7, v255, v4
	v_mul_lo_u32 v5, v255, v2
	s_waitcnt vmcnt(0)
	v_add_u32_e32 v8, 1, v6
	v_cmp_eq_u32_e32 vcc, v7, v8
	s_and_saveexec_b64 s[28:29], vcc
	s_cbranch_execz .Lxb_notlast
	buffer_wbl2 sc1
	s_waitcnt vmcnt(0)
	v_mov_b32_e32 v6, 1
	global_atomic_add v3, v6, s[6:7]
.Lxb_notlast:
	s_or_b64 exec, exec, s[28:29]
	s_mov_b32 s15, 0
.Lxb_poll:
	global_load_dword v6, v3, s[6:7] sc1
	s_waitcnt vmcnt(0)
	v_cmp_ge_u32_e32 vcc, v6, v5
	s_cbranch_vccnz .Lxb_done
	s_add_i32 s15, s15, 1
	s_cmp_lt_u32 s15, 0x400000
	s_cbranch_scc0 .Lxb_done
	s_sleep 1
	s_branch .Lxb_poll
.Lxb_done:
	s_waitcnt vmcnt(0) lgkmcnt(0)
	buffer_inv sc1
	s_waitcnt vmcnt(0)
	s_mov_b64 s[28:29], exec
	s_getpc_b64 s[98:99]

; __global__ void __launch_bounds__(NTHR, 2) mk_fwd(Params prm) {
	.amdhsa_kernel _ZN12_GLOBAL__N_16mk_fwdENS_6ParamsE
		.amdhsa_group_segment_fixed_size 72704
		.amdhsa_private_segment_fixed_size 0
		.amdhsa_kernarg_size 576
		.amdhsa_user_sgpr_count 2
		.amdhsa_user_sgpr_dispatch_ptr 0
		.amdhsa_user_sgpr_queue_ptr 0
		.amdhsa_user_sgpr_kernarg_segment_ptr 1
		.amdhsa_user_sgpr_dispatch_id 0
		.amdhsa_user_sgpr_kernarg_preload_length 0
		.amdhsa_user_sgpr_kernarg_preload_offset 0
		.amdhsa_user_sgpr_private_segment_size 0
		.amdhsa_uses_dynamic_stack 0
		.amdhsa_enable_private_segment 0
		.amdhsa_system_sgpr_workgroup_id_x 1
		.amdhsa_system_sgpr_workgroup_id_y 0
		.amdhsa_system_sgpr_workgroup_id_z 0
		.amdhsa_system_sgpr_workgroup_info 0
		.amdhsa_system_vgpr_workitem_id 0
		.amdhsa_next_free_vgpr 256
		.amdhsa_next_free_sgpr 102
		.amdhsa_accum_offset 256
		.amdhsa_reserve_vcc 1
		.amdhsa_float_round_mode_32 0
		.amdhsa_float_round_mode_16_64 0
		.amdhsa_float_denorm_mode_32 3
		.amdhsa_float_denorm_mode_16_64 3
		.amdhsa_dx10_clamp 1
		.amdhsa_ieee_mode 1
		.amdhsa_fp16_overflow 0
		.amdhsa_tg_split 0
		.amdhsa_exception_fp_ieee_invalid_op 0
		.amdhsa_exception_fp_denorm_src 0
		.amdhsa_exception_fp_ieee_div_zero 0
		.amdhsa_exception_fp_ieee_overflow 0
		.amdhsa_exception_fp_ieee_underflow 0
		.amdhsa_exception_fp_ieee_inexact 0
		.amdhsa_exception_int_div_zero 0
	.end_amdhsa_kernel

; __global__ void __launch_bounds__(NTHR, 2) mk_fwd(Params prm) {
amdhsa.kernels:
  - .agpr_count:     0
    .args:
      - .offset:         0
        .size:           320
        .value_kind:     by_value
      - .offset:         320
        .size:           4
        .value_kind:     hidden_block_count_x
      - .offset:         324
        .size:           4
        .value_kind:     hidden_block_count_y
      - .offset:         328
        .size:           4
        .value_kind:     hidden_block_count_z
      - .offset:         332
        .size:           2
        .value_kind:     hidden_group_size_x
      - .offset:         334
        .size:           2
        .value_kind:     hidden_group_size_y
      - .offset:         336
        .size:           2
        .value_kind:     hidden_group_size_z
      - .offset:         338
        .size:           2
        .value_kind:     hidden_remainder_x
      - .offset:         340
        .size:           2
        .value_kind:     hidden_remainder_y
      - .offset:         342
        .size:           2
        .value_kind:     hidden_remainder_z
      - .offset:         360
        .size:           8
        .value_kind:     hidden_global_offset_x
      - .offset:         368
        .size:           8
        .value_kind:     hidden_global_offset_y
      - .offset:         376
        .size:           8
        .value_kind:     hidden_global_offset_z
      - .offset:         384
        .size:           2
        .value_kind:     hidden_grid_dims
    .group_segment_fixed_size: 72704
    .kernarg_segment_align: 8
    .kernarg_segment_size: 576
    .language:       OpenCL C
    .language_version:
      - 2
      - 0
    .max_flat_workgroup_size: 256
    .name:           _ZN12_GLOBAL__N_16mk_fwdENS_6ParamsE
    .private_segment_fixed_size: 0
    .sgpr_count:     108
    .sgpr_spill_count: 144
    .symbol:         _ZN12_GLOBAL__N_16mk_fwdENS_6ParamsE.kd
    .uniform_work_group_size: 1
    .uses_dynamic_stack: false
    .vgpr_count:     256
    .vgpr_spill_count: 0
    .wavefront_size: 64
